# v82 + grid barrier between R1 and R2 replaced by an arrival counter (CNT written/read with sc1, TOPI/TOPW/RS3 are workgroup-local): no L2 write-back / two-level protocol for that seam
# baseline (speedup 1.0000x reference)
; template <int layer> __device__ __forceinline__ void layer_phases(const Ctx& c, unsigned char* lds) {
;     ...
;                         TOPI[mi * 2] = bi; TOPI[mi * 2 + 1] = ci; TOPW[mi * 2] = w0; TOPW[mi * 2 + 1] = w1; RS3[mi] = rs; atomicAdd(&cnt_l[bi], 1); atomicAdd(&cnt_l[ci], 1); }
;                     __syncthreads();
;                     if (tid < 8) CNT[blk * 8 + tid] = cnt_l[tid];
;                 }
.LBB0_1435:
	s_or_b64 exec, exec, s[20:21]
	s_waitcnt lgkmcnt(0)
	s_barrier
	s_and_saveexec_b64 s[20:21], s[4:5]
	s_cbranch_execz .LBB0_1406
	ds_read_b32 v4, v1 offset:32768
	v_ashrrev_i32_e32 v125, 31, v124
	v_lshl_add_u64 v[2:3], v[124:125], 2, s[28:29]
	s_waitcnt lgkmcnt(0)
	global_store_dword v[2:3], v4, off sc1
	s_branch .LBB0_1406

; __device__ __forceinline__ unsigned xb_ld(unsigned* p)              { return __hip_atomic_load(p, __ATOMIC_RELAXED, __HIP_MEMORY_SCOPE_AGENT); }
; __device__ __forceinline__ unsigned xb_add(unsigned* p, unsigned v) { return __hip_atomic_fetch_add(p, v, __ATOMIC_RELAXED, __HIP_MEMORY_SCOPE_AGENT); }
; #define XB_SPIN(cond, bar) do { unsigned _sp = 0; while (cond) { __builtin_amdgcn_s_sleep(1); \
;     if ((++_sp & 255u) == 0u) { if (xb_ld(&(bar)[XB_TMO])) break; if (_sp > XB_SPIN_CAP) { atomicAdd(&(bar)[XB_TMO], 1u); break; } } } } while (0)
; __device__ __forceinline__ void xcd_barrier(const XcdBarrier& b) {
;     asm volatile("s_waitcnt vmcnt(0)" ::: "memory");
;     __syncthreads();
;     if (threadIdx.x == 0) {
;         unsigned* bar = b.bar;
;         __builtin_amdgcn_s_waitcnt(0);
;         unsigned nloc = b.st[0], nx = b.st[1];
;         if (nloc == 0u) { xcd_barrier_complete(bar, b.x, nloc, nx); b.st[0] = nloc; b.st[1] = nx; }
;         const unsigned old = xb_add(&bar[XB_XSUB(b.x)], 1u);
;         const unsigned gen = old / nloc;
;         if (old + 1u == (gen + 1u) * nloc) {
;             __builtin_amdgcn_fence(__ATOMIC_RELEASE, "agent");
;             asm volatile("s_waitcnt vmcnt(0)" ::: "memory");
;             const unsigned og = xb_add(&bar[XB_TOP], 1u);
;             const unsigned tg = og / nx;
;             if (og + 1u == (tg + 1u) * nx) xb_add(&bar[XB_TOPGEN], 1u);
;             else XB_SPIN(xb_ld(&bar[XB_TOPGEN]) == tg, bar);
;             __builtin_amdgcn_fence(__ATOMIC_ACQUIRE, "agent");
;             xb_add(&bar[XB_XGEN(b.x)], 1u);
;             asm volatile("s_waitcnt vmcnt(0)" ::: "memory");
;         } else {
;             XB_SPIN(xb_ld(&bar[XB_XGEN(b.x)]) == gen, bar);
;             __builtin_amdgcn_fence(__ATOMIC_ACQUIRE, "agent");
;             asm volatile("s_waitcnt vmcnt(0)" ::: "memory");
;         }
;     }
;     __syncthreads();
; }
.LBB0_1439:
	v_readlane_b32 s4, v254, 0
	v_readlane_b32 s5, v254, 1
	s_cmp_gt_i32 s5, 23
	s_cselect_b64 s[4:5], -1, 0
	s_and_b64 s[0:1], s[0:1], s[4:5]
	s_andn2_b64 vcc, exec, s[0:1]
	v_readlane_b32 s6, v254, 2
	v_readlane_b32 s7, v254, 3
	s_cbranch_vccnz .LBB0_1493
	s_waitcnt vmcnt(0)
	s_waitcnt lgkmcnt(0)
	s_barrier
	s_mov_b64 s[0:1], exec
	v_readlane_b32 s2, v254, 7
	v_readlane_b32 s3, v254, 8
	s_and_b64 s[2:3], s[0:1], s[2:3]
	s_mov_b64 exec, s[2:3]
	s_cbranch_execz .LBB0_1492
	v_mov_b32_e32 v1, 0x4000
	v_mov_b32_e32 v2, 1
	global_atomic_add v1, v2, s[90:91]
	s_mov_b32 s2, 0
.Lr12_spin:
	global_load_dword v3, v1, s[90:91] sc1
	s_waitcnt vmcnt(0)
	v_readfirstlane_b32 s3, v3
	s_cmpk_gt_u32 s3, 0xff
	s_cbranch_scc1 .Lr12_done
	s_sleep 1
	s_add_i32 s2, s2, 1
	s_cmp_lt_u32 s2, 0x100000
	s_cbranch_scc1 .Lr12_spin
.Lr12_done:
.LBB0_1492:
	s_or_b64 exec, exec, s[0:1]
	s_waitcnt lgkmcnt(0)
	s_barrier

; template <int layer> __device__ __forceinline__ void layer_phases(const Ctx& c, unsigned char* lds) {
;     ...
;                     int cn[4];
; #pragma unroll
;                     for (int j = 0; j < 4; ++j) cn[j] = CNT[(4 * lane + j) * 8 + wave];
;                     int t = 0, pv = 0;
; #pragma unroll
;                     for (int j = 0; j < 4; ++j) { t += cn[j]; if (4 * lane + j < blk) pv += cn[j]; }
; #pragma unroll
;                     for (int st = 1; st < 64; st <<= 1) { t += __shfl_xor(t, st); pv += __shfl_xor(pv, st); }
;                     __syncthreads();
;                     if (lane == 0) { tot_l[wave] = t; pre_l[wave] = pv; }
;                     if (tid < 128) ent_l[tid] = ent;
;                     __syncthreads();
.LBB0_1501:
	s_or_b64 exec, exec, s[10:11]
	global_load_dword v42, v[6:7], off sc1
	global_load_dword v43, v[6:7], off offset:32 sc1
	global_load_dword v44, v[6:7], off offset:64 sc1
	global_load_dword v45, v[6:7], off offset:96 sc1
	v_cmp_gt_i32_e32 vcc, s42, v27
	s_waitcnt lgkmcnt(0)
	s_barrier
	s_waitcnt vmcnt(3)
	v_cndmask_b32_e32 v46, 0, v42, vcc
	v_cmp_gt_i32_e32 vcc, s42, v30
	s_waitcnt vmcnt(2)
	v_add_u32_e32 v42, v43, v42
	s_waitcnt vmcnt(0)
	v_add3_u32 v42, v42, v44, v45
	v_cndmask_b32_e32 v43, 0, v43, vcc
	v_cmp_gt_i32_e32 vcc, s42, v31
	v_add_u32_e32 v43, v43, v46
	s_nop 0
	v_cndmask_b32_e32 v47, 0, v44, vcc
	v_cmp_gt_i32_e32 vcc, s42, v32
	ds_bpermute_b32 v44, v33, v42
	s_waitcnt lgkmcnt(0)
	v_add_u32_e32 v42, v42, v44
	v_cndmask_b32_e32 v48, 0, v45, vcc
	v_add3_u32 v43, v43, v47, v48
	ds_bpermute_b32 v45, v33, v43
	ds_bpermute_b32 v44, v34, v42
	s_waitcnt lgkmcnt(1)
	v_add_u32_e32 v43, v43, v45
	ds_bpermute_b32 v45, v34, v43
	s_waitcnt lgkmcnt(1)
	v_add_u32_e32 v42, v44, v42
	ds_bpermute_b32 v44, v35, v42
	s_waitcnt lgkmcnt(1)
	v_add_u32_e32 v43, v45, v43
	ds_bpermute_b32 v45, v35, v43
	s_waitcnt lgkmcnt(1)
	v_add_u32_e32 v42, v44, v42
	ds_bpermute_b32 v44, v36, v42
	s_waitcnt lgkmcnt(1)
	v_add_u32_e32 v43, v45, v43
	ds_bpermute_b32 v45, v36, v43
	s_waitcnt lgkmcnt(1)
	v_add_u32_e32 v42, v44, v42
	ds_bpermute_b32 v44, v37, v42
	s_waitcnt lgkmcnt(1)
	v_add_u32_e32 v43, v45, v43
	ds_bpermute_b32 v45, v37, v43
	s_waitcnt lgkmcnt(1)
	v_add_u32_e32 v42, v44, v42
	ds_bpermute_b32 v44, v38, v42
	s_waitcnt lgkmcnt(1)
	v_add_u32_e32 v43, v45, v43
	ds_bpermute_b32 v45, v38, v43
	s_and_saveexec_b64 s[10:11], s[6:7]
	s_cbranch_execz .LBB0_1503
	s_waitcnt lgkmcnt(1)
	v_add_u32_e32 v42, v44, v42
	s_waitcnt lgkmcnt(0)
	v_add_u32_e32 v43, v45, v43
	v_mov_b32_e32 v44, s2
	ds_write2_b32 v44, v42, v43 offset1:8
